# MoE GEMM1/GEMM2 unit scheduler: expert lookup by five dependent LDS round trips replaced by one wave-wide ds_read + v_cmp + s_bcnt1; on top of v5
# speedup vs baseline: 1.0091x; 1.0091x over previous
.LBB0_1994:
	s_mov_b64 s[52:53], -1
	v_mbcnt_lo_u32_b32 v0, -1, 0
	v_mbcnt_hi_u32_b32 v0, -1, v0
	v_min_u32_e32 v0, 31, v0
	v_lshlrev_b32_e32 v0, 2, v0
	v_add_u32_e32 v0, 0x20400, v0
	ds_read_b32 v0, v0
	s_lshl_b32 s0, s40, 8
	s_waitcnt lgkmcnt(0)
	v_cmp_ge_i32_e32 vcc, s0, v0
	s_nop 3
	s_bcnt1_i32_b32 s44, vcc_lo
	s_add_i32 s44, s44, -1

.LBB0_2083:
	s_mov_b64 s[48:49], -1
	v_mbcnt_lo_u32_b32 v2, -1, 0
	v_mbcnt_hi_u32_b32 v2, -1, v2
	v_min_u32_e32 v2, 31, v2
	v_lshl_add_u32 v2, v2, 2, s52
	ds_read_b32 v2, v2
	s_lshl_b32 s0, s12, 8
	s_waitcnt lgkmcnt(0)
	v_cmp_ge_i32_e32 vcc, s0, v2
	s_nop 3
	s_bcnt1_i32_b32 s30, vcc_lo
	s_add_i32 s30, s30, -1
